# attention-A loop control lean: single s_cmp tile-barrier wait select, v_cmp_nge+vccnz rescale check, RESC blocks out of line, shorter loop tail; dtype comment added
# speedup vs baseline: 1.0701x; 1.0054x over previous
.Lattn_top:
	s_cmp_lg_u64 s[60:61], 0
	s_cbranch_scc1 .Ltb1_w0
	s_waitcnt vmcnt(1) lgkmcnt(0)

.LBB0_419:
	v_add_u32_e32 v225, s98, v163
	v_add_u32_e32 v226, s98, v220
	v_mfma_scale_f32_32x32x64_f8f6f4 v[112:127], v[228:233], v[182:187], v[80:95], v217, v216 op_sel_hi:[0,0,0] cbsz:2 blgp:2
	v_exp_f32_e32 v128, v128
	v_exp_f32_e32 v129, v129
	v_exp_f32_e32 v130, v130
	v_exp_f32_e32 v131, v131
	v_mfma_scale_f32_32x32x64_f8f6f4 v[96:111], v[234:239], v[182:187], v[80:95], v217, v216 op_sel_hi:[0,0,0] cbsz:2 blgp:2
	v_exp_f32_e32 v132, v132
	v_exp_f32_e32 v133, v133
	v_exp_f32_e32 v134, v134
	v_exp_f32_e32 v135, v135
	v_mfma_scale_f32_32x32x64_f8f6f4 v[112:127], v[240:245], v[176:181], v[112:127], v217, v216 op_sel_hi:[0,0,0] cbsz:2 blgp:2
	v_exp_f32_e32 v136, v136
	v_exp_f32_e32 v137, v137
	v_exp_f32_e32 v138, v138
	v_exp_f32_e32 v139, v139
	v_mfma_scale_f32_32x32x64_f8f6f4 v[96:111], v[246:251], v[176:181], v[96:111], v217, v216 op_sel_hi:[0,0,0] cbsz:2 blgp:2
	v_add_u32_e32 v200, s99, v223
	v_add_u32_e32 v201, s99, v224
	v_add_u32_e32 v202, s99, v221
	v_add_u32_e32 v203, s99, v222
	ds_read_b128 v[228:231], v200
	ds_read_b64 v[232:233], v201
	ds_read_b128 v[234:237], v200 offset:4096
	ds_read_b64 v[238:239], v201 offset:4096
	ds_read_b128 v[240:243], v202
	ds_read_b64 v[244:245], v203
	ds_read_b128 v[246:249], v202 offset:4096
	ds_read_b64 v[250:251], v203 offset:4096
	ds_read_b128 v[206:209], v225 offset:24576
	ds_read_b64 v[210:211], v226 offset:24576
	ds_read_b128 v[200:203], v225 offset:26624
	ds_read_b64 v[204:205], v226 offset:26624
	ds_read_b128 v[194:197], v225 offset:28672
	ds_read_b64 v[198:199], v226 offset:28672
	ds_read_b128 v[188:191], v225 offset:30720
	ds_read_b64 v[192:193], v226 offset:30720
	v_exp_f32_e32 v140, v140
	v_exp_f32_e32 v141, v141
	v_exp_f32_e32 v142, v142
	v_exp_f32_e32 v143, v143
	s_nop 0
	v_cvt_scalef32_2xpk16_bf6_f32 v[128:133], v[144:159], v[128:143], 1.0
	s_nop 1
	v_mfma_scale_f32_32x32x64_f8f6f4 v[64:79], v[128:133], v[168:173], v[64:79], v218, v218 op_sel_hi:[0,0,0] cbsz:3 blgp:2
	v_max_f32_e32 v225, v113, v113
	v_max_f32_e32 v226, v112, v112
	v_max_f32_e32 v225, v226, v225
	v_max3_f32 v225, v225, v114, v115
	s_waitcnt lgkmcnt(0)
	v_mfma_scale_f32_32x32x64_f8f6f4 v[0:15], v[128:133], v[206:211], v[0:15], v218, v217 op_sel_hi:[0,0,0] cbsz:3 blgp:2
	v_max3_f32 v225, v225, v116, v117
	v_max3_f32 v225, v225, v118, v119
	v_max3_f32 v225, v225, v120, v121
	v_max3_f32 v225, v225, v122, v123
	v_mfma_scale_f32_32x32x64_f8f6f4 v[48:63], v[128:133], v[200:205], v[48:63], v218, v217 op_sel_hi:[0,0,0] cbsz:3 blgp:2
	v_max3_f32 v225, v225, v124, v125
	v_max3_f32 v225, v225, v126, v127
	v_max3_f32 v225, v225, v96, v97
	v_max3_f32 v225, v225, v98, v99
	v_mfma_scale_f32_32x32x64_f8f6f4 v[32:47], v[128:133], v[194:199], v[32:47], v218, v217 op_sel_hi:[0,0,0] cbsz:3 blgp:2
	v_max3_f32 v225, v225, v100, v101
	v_max3_f32 v225, v225, v102, v103
	v_max3_f32 v225, v225, v104, v105
	v_max3_f32 v225, v225, v106, v107
	v_mfma_scale_f32_32x32x64_f8f6f4 v[16:31], v[128:133], v[188:193], v[16:31], v218, v217 op_sel_hi:[0,0,0] cbsz:3 blgp:2
	v_max3_f32 v225, v225, v108, v109
	v_max3_f32 v225, v225, v110, v111
	v_cmp_nge_f32_e32 vcc, s2, v225
	s_cbranch_vccnz .LBB0_444
.LBB0_424:
	v_exp_f32_e32 v112, v112
	v_exp_f32_e32 v113, v113
	v_exp_f32_e32 v114, v114
	v_exp_f32_e32 v115, v115
	v_exp_f32_e32 v116, v116
	v_exp_f32_e32 v117, v117
	v_exp_f32_e32 v118, v118
	v_exp_f32_e32 v119, v119
	v_exp_f32_e32 v120, v120
	v_exp_f32_e32 v121, v121
	v_exp_f32_e32 v122, v122
	v_exp_f32_e32 v123, v123
	v_exp_f32_e32 v124, v124
	v_exp_f32_e32 v125, v125
	v_exp_f32_e32 v126, v126
	v_exp_f32_e32 v127, v127
	s_cmp_lg_u64 s[60:61], 0
	s_cbranch_scc1 .Ltb2_w0
	s_waitcnt vmcnt(1) lgkmcnt(0)

.LBB0_437:
	v_add_u32_e32 v212, s100, v163
	v_add_u32_e32 v213, s100, v220
	v_mfma_scale_f32_32x32x64_f8f6f4 v[144:159], v[228:233], v[182:187], v[80:95], v217, v216 op_sel_hi:[0,0,0] cbsz:2 blgp:2
	v_exp_f32_e32 v96, v96
	v_exp_f32_e32 v97, v97
	v_exp_f32_e32 v98, v98
	v_exp_f32_e32 v99, v99
	v_mfma_scale_f32_32x32x64_f8f6f4 v[128:143], v[234:239], v[182:187], v[80:95], v217, v216 op_sel_hi:[0,0,0] cbsz:2 blgp:2
	v_exp_f32_e32 v100, v100
	v_exp_f32_e32 v101, v101
	v_exp_f32_e32 v102, v102
	v_exp_f32_e32 v103, v103
	v_mfma_scale_f32_32x32x64_f8f6f4 v[144:159], v[240:245], v[176:181], v[144:159], v217, v216 op_sel_hi:[0,0,0] cbsz:2 blgp:2
	v_exp_f32_e32 v104, v104
	v_exp_f32_e32 v105, v105
	v_exp_f32_e32 v106, v106
	v_exp_f32_e32 v107, v107
	v_mfma_scale_f32_32x32x64_f8f6f4 v[128:143], v[246:251], v[176:181], v[128:143], v217, v216 op_sel_hi:[0,0,0] cbsz:2 blgp:2
	v_add_u32_e32 v200, s98, v223
	v_add_u32_e32 v201, s98, v224
	v_add_u32_e32 v202, s98, v221
	v_add_u32_e32 v203, s98, v222
	ds_read_b128 v[228:231], v200
	ds_read_b64 v[232:233], v201
	ds_read_b128 v[234:237], v200 offset:4096
	ds_read_b64 v[238:239], v201 offset:4096
	ds_read_b128 v[240:243], v202
	ds_read_b64 v[244:245], v203
	ds_read_b128 v[246:249], v202 offset:4096
	ds_read_b64 v[250:251], v203 offset:4096
	ds_read_b128 v[206:209], v212 offset:24576
	ds_read_b64 v[210:211], v213 offset:24576
	ds_read_b128 v[200:203], v212 offset:26624
	ds_read_b64 v[204:205], v213 offset:26624
	ds_read_b128 v[194:197], v212 offset:28672
	ds_read_b64 v[198:199], v213 offset:28672
	ds_read_b128 v[188:191], v212 offset:30720
	ds_read_b64 v[192:193], v213 offset:30720
	v_exp_f32_e32 v108, v108
	v_exp_f32_e32 v109, v109
	v_exp_f32_e32 v110, v110
	v_exp_f32_e32 v111, v111
	s_nop 0
	v_cvt_scalef32_2xpk16_bf6_f32 v[96:101], v[112:127], v[96:111], 1.0
	s_nop 1
	v_mfma_scale_f32_32x32x64_f8f6f4 v[64:79], v[96:101], v[168:173], v[64:79], v218, v218 op_sel_hi:[0,0,0] cbsz:3 blgp:2
	v_max_f32_e32 v212, v145, v145
	v_max_f32_e32 v213, v144, v144
	v_max_f32_e32 v212, v213, v212
	v_max3_f32 v212, v212, v146, v147
	s_waitcnt lgkmcnt(0)
	v_mfma_scale_f32_32x32x64_f8f6f4 v[0:15], v[96:101], v[206:211], v[0:15], v218, v217 op_sel_hi:[0,0,0] cbsz:3 blgp:2
	v_max3_f32 v212, v212, v148, v149
	v_max3_f32 v212, v212, v150, v151
	v_max3_f32 v212, v212, v152, v153
	v_max3_f32 v212, v212, v154, v155
	v_mfma_scale_f32_32x32x64_f8f6f4 v[48:63], v[96:101], v[200:205], v[48:63], v218, v217 op_sel_hi:[0,0,0] cbsz:3 blgp:2
	v_max3_f32 v212, v212, v156, v157
	v_max3_f32 v212, v212, v158, v159
	v_max3_f32 v212, v212, v128, v129
	v_max3_f32 v212, v212, v130, v131
	v_mfma_scale_f32_32x32x64_f8f6f4 v[32:47], v[96:101], v[194:199], v[32:47], v218, v217 op_sel_hi:[0,0,0] cbsz:3 blgp:2
	v_max3_f32 v212, v212, v132, v133
	v_max3_f32 v212, v212, v134, v135
	v_max3_f32 v212, v212, v136, v137
	v_max3_f32 v212, v212, v138, v139
	v_mfma_scale_f32_32x32x64_f8f6f4 v[16:31], v[96:101], v[188:193], v[16:31], v218, v217 op_sel_hi:[0,0,0] cbsz:3 blgp:2
	v_max3_f32 v212, v212, v140, v141
	v_max3_f32 v212, v212, v142, v143
	v_cmp_nge_f32_e32 vcc, s2, v212
	s_cbranch_vccnz .LBB0_445
.LBB0_442:
	s_mov_b32 s101, s98
	s_mov_b32 s98, s99
	s_mov_b32 s99, s100
	s_mov_b32 s100, s101
	v_exp_f32_e32 v144, v144
	v_exp_f32_e32 v145, v145
	v_exp_f32_e32 v146, v146
	v_exp_f32_e32 v147, v147
	v_exp_f32_e32 v148, v148
	v_exp_f32_e32 v149, v149
	v_exp_f32_e32 v150, v150
	v_exp_f32_e32 v151, v151
	v_exp_f32_e32 v152, v152
	v_exp_f32_e32 v153, v153
	v_exp_f32_e32 v154, v154
	v_exp_f32_e32 v155, v155
	v_exp_f32_e32 v156, v156
	v_exp_f32_e32 v157, v157
	v_exp_f32_e32 v158, v158
	v_exp_f32_e32 v159, v159
	s_add_i32 s27, s27, -2
	s_add_u32 s10, s10, 0x4000
	s_addc_u32 s11, s11, 0
	s_add_i32 s1, s1, 2
	s_cmpk_gt_u32 s1, 0xff
	s_cbranch_scc0 .Lattn_top
	s_branch .LBB0_446

.Ltb1_w0:
	s_waitcnt vmcnt(0) lgkmcnt(0)
	s_branch .LBB0_417

.LBB0_420:
	v_cmp_gt_f32_e32 vcc, 1.0, v166
	s_cbranch_vccz .LBB0_424
	v_mbcnt_lo_u32_b32 v128, -1, 0
	v_mbcnt_hi_u32_b32 v128, -1, v128
	s_nop 0
	v_cmp_gt_u32_e32 vcc, 32, v128
	s_and_saveexec_b64 s[12:13], vcc
	v_lshl_add_u32 v129, v128, 2, s86
	ds_write_b32 v129, v166 offset:49152
	s_or_b64 exec, exec, s[12:13]
	v_ashrrev_i32_e32 v128, 3, v128
	v_lshlrev_b32_e32 v128, 2, v128
	v_and_b32_e32 v128, -16, v128
	s_waitcnt lgkmcnt(0)
	v_add_u32_e32 v140, s86, v128
	ds_read_b128 v[128:131], v140 offset:49248
	ds_read_b128 v[132:135], v140 offset:49216
	ds_read_b128 v[136:139], v140 offset:49184
	ds_read_b128 v[140:143], v140 offset:49152
	s_waitcnt lgkmcnt(0)
	v_pk_mul_f32 v[12:13], v[12:13], v[128:129]
	v_pk_mul_f32 v[8:9], v[8:9], v[132:133]
	v_pk_mul_f32 v[4:5], v[4:5], v[136:137]
	v_pk_mul_f32 v[14:15], v[14:15], v[130:131]
	v_pk_mul_f32 v[10:11], v[10:11], v[134:135]
	v_pk_mul_f32 v[6:7], v[6:7], v[138:139]
	v_pk_mul_f32 v[2:3], v[2:3], v[142:143]
	v_pk_mul_f32 v[0:1], v[0:1], v[140:141]
	v_pk_mul_f32 v[60:61], v[60:61], v[128:129]
	v_pk_mul_f32 v[56:57], v[56:57], v[132:133]
	v_pk_mul_f32 v[52:53], v[52:53], v[136:137]
	v_pk_mul_f32 v[62:63], v[62:63], v[130:131]
	v_pk_mul_f32 v[58:59], v[58:59], v[134:135]
	v_pk_mul_f32 v[54:55], v[54:55], v[138:139]
	v_pk_mul_f32 v[50:51], v[50:51], v[142:143]
	v_pk_mul_f32 v[48:49], v[48:49], v[140:141]
	v_pk_mul_f32 v[44:45], v[44:45], v[128:129]
	v_pk_mul_f32 v[40:41], v[40:41], v[132:133]
	v_pk_mul_f32 v[36:37], v[36:37], v[136:137]
	v_pk_mul_f32 v[46:47], v[46:47], v[130:131]
	v_pk_mul_f32 v[42:43], v[42:43], v[134:135]
	v_pk_mul_f32 v[38:39], v[38:39], v[138:139]
	v_pk_mul_f32 v[34:35], v[34:35], v[142:143]
	v_pk_mul_f32 v[32:33], v[32:33], v[140:141]
	v_pk_mul_f32 v[28:29], v[28:29], v[128:129]
	v_pk_mul_f32 v[24:25], v[24:25], v[132:133]
	v_pk_mul_f32 v[20:21], v[20:21], v[136:137]
	v_pk_mul_f32 v[30:31], v[30:31], v[130:131]
	v_pk_mul_f32 v[26:27], v[26:27], v[134:135]
	v_pk_mul_f32 v[22:23], v[22:23], v[138:139]
	v_pk_mul_f32 v[18:19], v[18:19], v[142:143]
	v_pk_mul_f32 v[16:17], v[16:17], v[140:141]
	v_pk_mul_f32 v[76:77], v[76:77], v[128:129]
	v_pk_mul_f32 v[72:73], v[72:73], v[132:133]
	v_pk_mul_f32 v[68:69], v[68:69], v[136:137]
	v_pk_mul_f32 v[78:79], v[78:79], v[130:131]
	v_pk_mul_f32 v[74:75], v[74:75], v[134:135]
	v_pk_mul_f32 v[70:71], v[70:71], v[138:139]
	v_pk_mul_f32 v[66:67], v[66:67], v[142:143]
	v_pk_mul_f32 v[64:65], v[64:65], v[140:141]
	s_branch .LBB0_424
.LBB0_438:
	v_cmp_gt_f32_e32 vcc, 1.0, v166
	s_cbranch_vccz .LBB0_442
	v_mbcnt_lo_u32_b32 v96, -1, 0
	v_mbcnt_hi_u32_b32 v96, -1, v96
	s_nop 0
	v_cmp_gt_u32_e32 vcc, 32, v96
	s_and_saveexec_b64 s[12:13], vcc
	v_lshl_add_u32 v97, v96, 2, s86
	ds_write_b32 v97, v166 offset:49152
	s_or_b64 exec, exec, s[12:13]
	v_ashrrev_i32_e32 v96, 3, v96
	v_lshlrev_b32_e32 v96, 2, v96
	v_and_b32_e32 v96, -16, v96
	s_waitcnt lgkmcnt(0)
	v_add_u32_e32 v108, s86, v96
	ds_read_b128 v[96:99], v108 offset:49248
	ds_read_b128 v[100:103], v108 offset:49216
	ds_read_b128 v[104:107], v108 offset:49184
	ds_read_b128 v[108:111], v108 offset:49152
	s_waitcnt lgkmcnt(0)
	v_pk_mul_f32 v[12:13], v[12:13], v[96:97]
	v_pk_mul_f32 v[8:9], v[8:9], v[100:101]
	v_pk_mul_f32 v[4:5], v[4:5], v[104:105]
	v_pk_mul_f32 v[14:15], v[14:15], v[98:99]
	v_pk_mul_f32 v[10:11], v[10:11], v[102:103]
	v_pk_mul_f32 v[6:7], v[6:7], v[106:107]
	v_pk_mul_f32 v[2:3], v[2:3], v[110:111]
	v_pk_mul_f32 v[0:1], v[0:1], v[108:109]
	v_pk_mul_f32 v[60:61], v[60:61], v[96:97]
	v_pk_mul_f32 v[56:57], v[56:57], v[100:101]
	v_pk_mul_f32 v[52:53], v[52:53], v[104:105]
	v_pk_mul_f32 v[62:63], v[62:63], v[98:99]
	v_pk_mul_f32 v[58:59], v[58:59], v[102:103]
	v_pk_mul_f32 v[54:55], v[54:55], v[106:107]
	v_pk_mul_f32 v[50:51], v[50:51], v[110:111]
	v_pk_mul_f32 v[48:49], v[48:49], v[108:109]
	v_pk_mul_f32 v[44:45], v[44:45], v[96:97]
	v_pk_mul_f32 v[40:41], v[40:41], v[100:101]
	v_pk_mul_f32 v[36:37], v[36:37], v[104:105]
	v_pk_mul_f32 v[46:47], v[46:47], v[98:99]
	v_pk_mul_f32 v[42:43], v[42:43], v[102:103]
	v_pk_mul_f32 v[38:39], v[38:39], v[106:107]
	v_pk_mul_f32 v[34:35], v[34:35], v[110:111]
	v_pk_mul_f32 v[32:33], v[32:33], v[108:109]
	v_pk_mul_f32 v[28:29], v[28:29], v[96:97]
	v_pk_mul_f32 v[24:25], v[24:25], v[100:101]
	v_pk_mul_f32 v[20:21], v[20:21], v[104:105]
	v_pk_mul_f32 v[30:31], v[30:31], v[98:99]
	v_pk_mul_f32 v[26:27], v[26:27], v[102:103]
	v_pk_mul_f32 v[22:23], v[22:23], v[106:107]
	v_pk_mul_f32 v[18:19], v[18:19], v[110:111]
	v_pk_mul_f32 v[16:17], v[16:17], v[108:109]
	v_pk_mul_f32 v[76:77], v[76:77], v[96:97]
	v_pk_mul_f32 v[72:73], v[72:73], v[100:101]
	v_pk_mul_f32 v[68:69], v[68:69], v[104:105]
	v_pk_mul_f32 v[78:79], v[78:79], v[98:99]
	v_pk_mul_f32 v[74:75], v[74:75], v[102:103]
	v_pk_mul_f32 v[70:71], v[70:71], v[106:107]
	v_pk_mul_f32 v[66:67], v[66:67], v[110:111]
	v_pk_mul_f32 v[64:65], v[64:65], v[108:109]
	s_branch .LBB0_442
